# baseline (speedup 1.0000x reference)
_Z11attn_kernelILi0EEvPKDF16_S1_S1_PKfS3_PfPDF16_:
	s_cmp_ge_u32 s2, 0x100
	s_cbranch_scc0 .Lprio_skip
	s_setprio 3
.Lprio_skip:
	v_readfirstlane_b32 s3, v0
	s_lshr_b32 s14, s3, 6
	s_lshl_b32 s3, s2, 7
	s_lshr_b32 s12, s2, 4
	s_and_b32 s3, s3, 0x780
	s_lshl_b32 s4, s14, 5
	s_mov_b32 s13, 0
	s_load_dwordx4 s[8:11], s[0:1], 0x0
	s_load_dwordx2 s[18:19], s[0:1], 0x10
	s_add_i32 s3, s4, s3
	s_lshl_b64 s[4:5], s[12:13], 11
	s_add_u32 s16, s4, s3
	s_addc_u32 s17, s5, 0
	s_lshl_b64 s[4:5], s[16:17], 7
	v_and_b32_e32 v164, 31, v0
	s_waitcnt lgkmcnt(0)
	s_add_u32 s4, s8, s4
	v_bfe_u32 v72, v0, 5, 1
	s_addc_u32 s5, s9, s5
	s_lshl_b64 s[22:23], s[12:13], 18
	v_lshlrev_b32_e32 v128, 7, v164
	v_mov_b32_e32 v129, 0
	s_add_u32 s8, s10, s22
	v_lshl_add_u64 v[2:3], s[4:5], 0, v[128:129]
	v_lshlrev_b32_e32 v128, 4, v72
	s_addc_u32 s9, s11, s23
	v_lshl_add_u64 v[10:11], v[2:3], 0, v[128:129]
	v_or_b32_e32 v12, 0x100, v0
	v_lshlrev_b32_e32 v128, 4, v0
	v_lshlrev_b32_e32 v44, 4, v12
	global_load_dwordx4 v[2:5], v128, s[8:9]
	global_load_dwordx4 v[6:9], v44, s[8:9]
	v_lshlrev_b32_e32 v79, 3, v0
	s_movk_i32 s4, 0x48
	v_lshrrev_b32_e32 v73, 3, v0
	v_and_b32_e32 v74, 56, v79
	v_lshrrev_b32_e32 v75, 3, v12
	v_mad_u32_u24 v165, v75, s4, v74
	v_mad_u32_u24 v166, v73, s4, v74
	global_load_dwordx4 v[108:111], v[10:11], off
	global_load_dwordx4 v[104:107], v[10:11], off offset:32
	global_load_dwordx4 v[100:103], v[10:11], off offset:64
	global_load_dwordx4 v[96:99], v[10:11], off offset:96
	v_mov_b32_e32 v86, v44
	s_add_u32 s24, s8, 0x2000
	s_addc_u32 s25, s9, 0
	global_load_dwordx4 v[120:123], v128, s[24:25]
	global_load_dwordx4 v[124:127], v44, s[24:25]
	s_add_u32 s24, s24, 0x2000
	s_addc_u32 s25, s25, 0
	global_load_dwordx4 v[146:149], v128, s[24:25]
	global_load_dwordx4 v[150:153], v44, s[24:25]
	s_add_u32 s24, s24, 0x2000
	s_addc_u32 s25, s25, 0
	global_load_dwordx4 v[154:157], v128, s[24:25]
	global_load_dwordx4 v[158:161], v44, s[24:25]
	s_add_u32 s24, s24, 0x2000
	s_addc_u32 s25, s25, 0
	s_add_u32 s4, s8, 0x2000
	v_lshlrev_b32_e32 v13, 1, v166
	s_addc_u32 s5, s9, 0
	v_lshlrev_b32_e32 v14, 1, v165
	v_lshlrev_b32_e32 v1, 3, v72
	v_mul_u32_u24_e32 v76, 0x48, v164
	v_lshlrev_b32_e32 v80, 3, v12
	v_mov_b32_e32 v45, v129
	s_mov_b32 s15, 1
	v_add_u32_e32 v77, 0x6000, v13
	v_add_u32_e32 v78, 0x6000, v14
	s_waitcnt vmcnt(11)
	ds_write_b128 v13, v[2:5] offset:24576
	s_waitcnt vmcnt(10)
	ds_write_b128 v14, v[6:9] offset:24576
	s_waitcnt lgkmcnt(0)
	s_barrier
	s_load_dwordx4 s[4:7], s[0:1], 0x28
	v_add_lshl_u32 v3, v1, v76, 1
	v_lshl_add_u64 v[68:69], s[8:9], 0, v[44:45]
	v_lshl_add_u64 v[66:67], s[8:9], 0, v[128:129]
	v_add_u32_e32 v167, 0x6000, v3
	v_mov_b32_e32 v87, v3
	v_lshlrev_b32_e32 v88, 1, v166
	v_lshlrev_b32_e32 v89, 1, v165
	s_lshl_b64 s[20:21], s[12:13], 17
	v_mov_b32_e32 v81, 0
	v_mov_b32_e32 v82, 0
	v_mov_b32_e32 v130, 0
	v_mov_b32_e32 v131, 0
	v_mov_b32_e32 v132, 0
	v_mov_b32_e32 v133, 0
	v_mov_b32_e32 v134, 0
	v_mov_b32_e32 v135, 0
	v_mov_b32_e32 v136, 0
	v_mov_b32_e32 v137, 0
	v_mov_b32_e32 v138, 0
	v_mov_b32_e32 v139, 0
	v_mov_b32_e32 v140, 0
	v_mov_b32_e32 v141, 0
	v_mov_b32_e32 v142, 0
	v_mov_b32_e32 v143, 0
	v_mov_b32_e32 v144, 0
	v_mov_b32_e32 v145, 0
	v_mov_b32_e32 v34, 0xff800000
	v_mov_b32_e32 v35, v34
	v_mov_b32_e32 v36, v34
	v_mov_b32_e32 v37, v34
	v_mov_b32_e32 v38, v34
	v_mov_b32_e32 v39, v34
	v_mov_b32_e32 v40, v34
	v_mov_b32_e32 v41, v34
	v_mov_b32_e32 v42, v34
	v_mov_b32_e32 v43, v34
	v_mov_b32_e32 v44, v34
	v_mov_b32_e32 v45, v34
	v_mov_b32_e32 v46, v34
	v_mov_b32_e32 v47, v34
	v_mov_b32_e32 v48, v34
	v_mov_b32_e32 v49, v34
	v_mov_b32_e32 v50, v34
	v_mov_b32_e32 v51, v34
	v_mov_b32_e32 v52, v34
	v_mov_b32_e32 v53, v34
	v_mov_b32_e32 v54, v34
	v_mov_b32_e32 v55, v34
	v_mov_b32_e32 v56, v34
	v_mov_b32_e32 v57, v34
	v_mov_b32_e32 v58, v34
	v_mov_b32_e32 v59, v34
	v_mov_b32_e32 v60, v34
	v_mov_b32_e32 v61, v34
	v_mov_b32_e32 v62, v34
	v_mov_b32_e32 v63, v34
	v_mov_b32_e32 v64, v34
	v_mov_b32_e32 v65, v34
	s_mov_b32 s11, 0xff800000
	s_mov_b32 s15, 0
	s_waitcnt vmcnt(4) lgkmcnt(0)
	ds_write_b128 v77, v[120:123] offset:9216
	ds_write_b128 v78, v[124:127] offset:9216
	s_waitcnt lgkmcnt(0)
	s_barrier

.Lp1_fin:
	s_lshl_b64 s[0:1], s[20:21], 1
	s_add_u32 s0, s18, s0
	s_addc_u32 s1, s19, s1
	global_load_dwordx4 v[2:5], v[66:67], off
	global_load_dwordx4 v[6:9], v[68:69], off
	v_lshlrev_b32_e32 v10, 1, v79
	global_load_dwordx4 v[10:13], v10, s[0:1]
	v_lshlrev_b32_e32 v14, 1, v80
	global_load_dwordx4 v[14:17], v14, s[0:1]
	v_mov_b32_e32 v200, 0
	v_mov_b32_e32 v201, 0
	v_mov_b32_e32 v202, 0
	v_mov_b32_e32 v83, 0
	v_exp_f32_e32 v34, v34
	v_exp_f32_e32 v35, v35
	v_add_f32_e32 v200, v200, v34
	v_exp_f32_e32 v36, v36
	v_add_f32_e32 v201, v201, v35
	v_exp_f32_e32 v37, v37
	v_add_f32_e32 v202, v202, v36
	v_exp_f32_e32 v38, v38
	v_add_f32_e32 v83, v83, v37
	v_exp_f32_e32 v39, v39
	v_add_f32_e32 v200, v200, v38
	v_exp_f32_e32 v40, v40
	v_add_f32_e32 v201, v201, v39
	v_exp_f32_e32 v41, v41
	v_add_f32_e32 v202, v202, v40
	v_exp_f32_e32 v42, v42
	v_add_f32_e32 v83, v83, v41
	v_exp_f32_e32 v43, v43
	v_add_f32_e32 v200, v200, v42
	v_exp_f32_e32 v44, v44
	v_add_f32_e32 v201, v201, v43
	v_exp_f32_e32 v45, v45
	v_add_f32_e32 v202, v202, v44
	v_exp_f32_e32 v46, v46
	v_add_f32_e32 v83, v83, v45
	v_exp_f32_e32 v47, v47
	v_add_f32_e32 v200, v200, v46
	v_exp_f32_e32 v48, v48
	v_add_f32_e32 v201, v201, v47
	v_exp_f32_e32 v49, v49
	v_add_f32_e32 v202, v202, v48
	v_exp_f32_e32 v50, v50
	v_add_f32_e32 v83, v83, v49
	v_exp_f32_e32 v51, v51
	v_add_f32_e32 v200, v200, v50
	v_exp_f32_e32 v52, v52
	v_add_f32_e32 v201, v201, v51
	v_exp_f32_e32 v53, v53
	v_add_f32_e32 v202, v202, v52
	v_exp_f32_e32 v54, v54
	v_add_f32_e32 v83, v83, v53
	v_exp_f32_e32 v55, v55
	v_add_f32_e32 v200, v200, v54
	v_exp_f32_e32 v56, v56
	v_add_f32_e32 v201, v201, v55
	v_exp_f32_e32 v57, v57
	v_add_f32_e32 v202, v202, v56
	v_exp_f32_e32 v58, v58
	v_add_f32_e32 v83, v83, v57
	v_exp_f32_e32 v59, v59
	v_add_f32_e32 v200, v200, v58
	v_exp_f32_e32 v60, v60
	v_add_f32_e32 v201, v201, v59
	v_exp_f32_e32 v61, v61
	v_add_f32_e32 v202, v202, v60
	v_exp_f32_e32 v62, v62
	v_add_f32_e32 v83, v83, v61
	v_exp_f32_e32 v63, v63
	v_add_f32_e32 v200, v200, v62
	v_exp_f32_e32 v64, v64
	v_add_f32_e32 v201, v201, v63
	v_exp_f32_e32 v65, v65
	v_add_f32_e32 v202, v202, v64
	v_add_f32_e32 v83, v83, v65
	v_add_f32_e32 v200, v200, v201
	v_add_f32_e32 v202, v202, v83
	v_add_f32_e32 v200, v200, v202
	v_add_f32_e32 v82, v82, v200
	s_setprio 0
	s_barrier
	v_mbcnt_lo_u32_b32 v21, -1, 0
	v_mbcnt_hi_u32_b32 v21, -1, v21
	v_and_b32_e32 v23, 64, v21
	v_xor_b32_e32 v22, 32, v21
	v_add_u32_e32 v24, 64, v23
	v_cmp_lt_i32_e32 vcc, v22, v24
	v_cndmask_b32_e32 v21, v21, v22, vcc
	v_lshlrev_b32_e32 v21, 2, v21
	ds_bpermute_b32 v22, v21, v81
	v_mov_b32_e32 v18, v82
	ds_bpermute_b32 v19, v21, v18
	v_max_f32_e32 v21, v81, v81
	s_mov_b32 s15, 0
	s_waitcnt lgkmcnt(1)
	v_max_f32_e32 v20, v22, v22
	v_max_f32_e32 v20, v21, v20
	v_sub_f32_e32 v22, v22, v20
	v_sub_f32_e32 v21, v81, v20
	v_exp_f32_e32 v22, v22
	v_exp_f32_e32 v21, v21
	s_lshl_b64 s[18:19], s[14:15], 18
	v_mov_b32_e32 v131, 0
	s_waitcnt lgkmcnt(0)
	v_mul_f32_e32 v19, v22, v19
	v_fmac_f32_e32 v19, v18, v21
	v_div_scale_f32 v18, s[10:11], v19, v19, 1.0
	s_movk_i32 s10, 0x60
	s_nop 0
	v_mad_u32_u24 v188, v73, s10, v74
	v_mad_u32_u24 v189, v75, s10, v74
	s_waitcnt vmcnt(3)
	ds_write_b128 v77, v[2:5]
	s_waitcnt vmcnt(2)
	ds_write_b128 v78, v[6:9]
	v_lshlrev_b32_e32 v2, 1, v188
	s_waitcnt vmcnt(1)
	ds_write_b128 v2, v[10:13]
	v_lshlrev_b32_e32 v2, 1, v189
	s_mul_i32 s10, s14, 0x1200
	s_waitcnt vmcnt(0)
	ds_write_b128 v2, v[14:17]
	s_add_i32 s10, s10, 0xa800
	v_lshrrev_b32_e32 v2, 2, v0
	v_and_or_b32 v3, v2, 3, v1
	s_movk_i32 s11, 0x48
	v_mov_b32_e32 v5, s10
	v_add_u32_e32 v4, s10, v76
	v_mad_u32_u24 v5, v3, s11, v5
	s_lshl_b64 s[10:11], s[12:13], 24
	s_and_b32 s13, s2, 15
	s_lshl_b32 s13, s13, 20
	v_and_b32_e32 v0, 3, v0
	s_or_b32 s10, s10, s13
	v_and_or_b32 v0, v2, 4, v0
	s_add_u32 s10, s10, s18
	v_lshlrev_b32_e32 v0, 3, v0
	v_mul_u32_u24_e32 v2, 0xc0, v3
	v_lshlrev_b32_e32 v3, 13, v72
	s_addc_u32 s11, s11, s19
	v_or_b32_e32 v185, v2, v0
	v_or_b32_e32 v2, v3, v164
	s_add_u32 s10, s4, s10
	v_lshlrev_b32_e32 v130, 2, v2
	s_addc_u32 s11, s5, s11
	v_lshl_add_u64 v[2:3], s[10:11], 0, v[130:131]
	s_mov_b64 s[18:19], 0x80
	v_lshl_add_u64 v[132:133], v[2:3], 0, s[18:19]
	v_or_b32_e32 v2, 0x36000, v130
	v_mov_b32_e32 v3, v131
	v_lshl_add_u64 v[134:135], s[10:11], 0, v[2:3]
	v_or_b32_e32 v2, 0x2000, v130
	v_lshl_add_u64 v[2:3], s[10:11], 0, v[2:3]
	v_lshl_add_u64 v[136:137], v[2:3], 0, s[18:19]
	v_or_b32_e32 v2, 0x34000, v130
	v_mov_b32_e32 v3, v131
	v_rcp_f32_e32 v21, v18
	v_lshl_add_u64 v[138:139], s[10:11], 0, v[2:3]
	v_or_b32_e32 v2, 0x4000, v130
	v_lshl_add_u64 v[2:3], s[10:11], 0, v[2:3]
	v_lshl_add_u64 v[140:141], v[2:3], 0, s[18:19]
	v_or_b32_e32 v2, 0x32000, v130
	v_mov_b32_e32 v3, v131
	v_lshl_add_u64 v[142:143], s[10:11], 0, v[2:3]
	v_or_b32_e32 v2, 0x6000, v130
	v_fma_f32 v22, -v18, v21, 1.0
	v_lshl_add_u64 v[2:3], s[10:11], 0, v[2:3]
	v_fmac_f32_e32 v21, v22, v21
	v_div_scale_f32 v22, vcc, 1.0, v19, 1.0
	v_lshl_add_u64 v[144:145], v[2:3], 0, s[18:19]
	v_or_b32_e32 v2, 0x30000, v130
	v_mov_b32_e32 v3, v131
	v_mul_f32_e32 v24, v22, v21
	v_lshl_add_u64 v[146:147], s[10:11], 0, v[2:3]
	v_or_b32_e32 v2, 0x10000, v130
	v_fma_f32 v25, -v18, v24, v22
	v_lshl_add_u64 v[2:3], s[10:11], 0, v[2:3]
	v_fmac_f32_e32 v24, v25, v21
	v_lshl_add_u64 v[148:149], v[2:3], 0, s[18:19]
	v_or_b32_e32 v2, 0x26000, v130
	v_mov_b32_e32 v3, v131
	v_fma_f32 v18, -v18, v24, v22
	v_lshl_add_u64 v[150:151], s[10:11], 0, v[2:3]
	v_or_b32_e32 v2, 0x12000, v130
	v_div_fmas_f32 v18, v18, v21, v24
	v_lshlrev_b32_e32 v184, 2, v72
	v_lshl_add_u64 v[2:3], s[10:11], 0, v[2:3]
	v_div_fixup_f32 v18, v18, v19, 1.0
	v_or_b32_e32 v19, v184, v23
	v_lshl_add_u64 v[152:153], v[2:3], 0, s[18:19]
	v_or_b32_e32 v2, 0x24000, v130
	v_mov_b32_e32 v3, v131
	v_lshlrev_b32_e32 v19, 2, v19
	v_lshl_add_u64 v[154:155], s[10:11], 0, v[2:3]
	v_or_b32_e32 v2, 0x14000, v130
	ds_bpermute_b32 v33, v19, v20 offset:36
	ds_bpermute_b32 v32, v19, v20 offset:40
	ds_bpermute_b32 v35, v19, v20 offset:44
	ds_bpermute_b32 v34, v19, v20 offset:64
	ds_bpermute_b32 v37, v19, v20 offset:68
	ds_bpermute_b32 v36, v19, v20 offset:72
	ds_bpermute_b32 v39, v19, v20 offset:76
	ds_bpermute_b32 v38, v19, v20 offset:96
	ds_bpermute_b32 v41, v19, v20 offset:100
	ds_bpermute_b32 v40, v19, v20 offset:104
	ds_bpermute_b32 v43, v19, v20 offset:108
	v_lshl_add_u64 v[2:3], s[10:11], 0, v[2:3]
	ds_bpermute_b32 v46, v19, v20 offset:32
	ds_bpermute_b32 v47, v19, v20 offset:12
	ds_bpermute_b32 v42, v19, v20 offset:8
	ds_bpermute_b32 v45, v19, v20 offset:4
	ds_bpermute_b32 v44, v19, v20
	ds_bpermute_b32 v183, v19, v18
	ds_bpermute_b32 v182, v19, v18 offset:4
	ds_bpermute_b32 v181, v19, v18 offset:8
	ds_bpermute_b32 v180, v19, v18 offset:12
	ds_bpermute_b32 v179, v19, v18 offset:32
	ds_bpermute_b32 v178, v19, v18 offset:36
	ds_bpermute_b32 v177, v19, v18 offset:40
	ds_bpermute_b32 v176, v19, v18 offset:44
	ds_bpermute_b32 v175, v19, v18 offset:64
	ds_bpermute_b32 v174, v19, v18 offset:68
	ds_bpermute_b32 v173, v19, v18 offset:72
	ds_bpermute_b32 v172, v19, v18 offset:76
	ds_bpermute_b32 v171, v19, v18 offset:96
	ds_bpermute_b32 v170, v19, v18 offset:100
	ds_bpermute_b32 v169, v19, v18 offset:104
	ds_bpermute_b32 v168, v19, v18 offset:108
	v_lshl_add_u64 v[156:157], v[2:3], 0, s[18:19]
	v_or_b32_e32 v2, 0x22000, v130
	v_mov_b32_e32 v3, v131
	v_lshl_add_u64 v[158:159], s[10:11], 0, v[2:3]
	v_or_b32_e32 v2, 0x16000, v130
	v_lshl_add_u64 v[2:3], s[10:11], 0, v[2:3]
	v_lshl_add_u64 v[160:161], v[2:3], 0, s[18:19]
	v_or_b32_e32 v2, 0x20000, v130
	v_mov_b32_e32 v3, v131
	v_add_u32_e32 v187, v4, v1
	v_lshl_add_u64 v[162:163], s[10:11], 0, v[2:3]
	s_mov_b64 s[10:11], 0
	s_movk_i32 s13, 0x3000
	s_waitcnt lgkmcnt(14)
	v_xor_b32_e32 v63, 0x80000000, v43
	v_xor_b32_e32 v62, 0x80000000, v40
	v_xor_b32_e32 v61, 0x80000000, v41
	v_xor_b32_e32 v60, 0x80000000, v38
	v_xor_b32_e32 v59, 0x80000000, v39
	v_xor_b32_e32 v58, 0x80000000, v36
	v_xor_b32_e32 v57, 0x80000000, v37
	v_xor_b32_e32 v56, 0x80000000, v34
	v_xor_b32_e32 v55, 0x80000000, v35
	v_xor_b32_e32 v54, 0x80000000, v32
	v_xor_b32_e32 v53, 0x80000000, v33
	v_add_u32_e32 v186, v5, v0
	v_xor_b32_e32 v52, 0x80000000, v46
	v_xor_b32_e32 v51, 0x80000000, v47
	v_xor_b32_e32 v50, 0x80000000, v42
	v_xor_b32_e32 v49, 0x80000000, v45
	v_xor_b32_e32 v48, 0x80000000, v44
	v_mov_b32_e32 v0, v131
	v_mov_b32_e32 v1, v131
	v_mov_b32_e32 v2, v131
	v_mov_b32_e32 v4, v131
	v_mov_b32_e32 v5, v131
	v_mov_b32_e32 v6, v131
	v_mov_b32_e32 v7, v131
	v_mov_b32_e32 v8, v131
	v_mov_b32_e32 v9, v131
	v_mov_b32_e32 v10, v131
	v_mov_b32_e32 v11, v131
	v_mov_b32_e32 v12, v131
	v_mov_b32_e32 v13, v131
	v_mov_b32_e32 v14, v131
	v_mov_b32_e32 v15, v131
	v_mov_b32_e32 v16, v131
	v_mov_b32_e32 v17, v131
	v_mov_b32_e32 v18, v131
	v_mov_b32_e32 v19, v131
	v_mov_b32_e32 v20, v131
	v_mov_b32_e32 v21, v131
	v_mov_b32_e32 v22, v131
	v_mov_b32_e32 v23, v131
	v_mov_b32_e32 v24, v131
	v_mov_b32_e32 v25, v131
	v_mov_b32_e32 v26, v131
	v_mov_b32_e32 v27, v131
	v_mov_b32_e32 v28, v131
	v_mov_b32_e32 v29, v131
	v_mov_b32_e32 v30, v131
	v_mov_b32_e32 v31, v131
	v_add_u32_e32 v131, 0x800, v187
	s_waitcnt lgkmcnt(0)
	s_barrier
